# v51 stack + hy_prep conv-weight loads issued before the first wait
# speedup vs baseline: 1.0144x; 1.0144x over previous
; #define GAS __attribute__((address_space(1)))
; __device__ __forceinline__ unsigned pk2(float lo, float hi) { const m_f32x2 v = {lo, hi}; return __builtin_bit_cast(unsigned, __builtin_convertvector(v, m_bf16x2)); }
; __device__ __forceinline__ float bfe(const v4u& w, int e) { const unsigned u = (e & 1) ? (w[e >> 1] & 0xffff0000u) : (w[e >> 1] << 16); return __uint_as_float(u); }
; template <int EH> __device__ __forceinline__ void hy_conv4x4(const v4u (&rows)[6], const GAS float* w, const GAS float* bias, float (&u)[4][4]) {
;     const f32x4 w0 = *(const GAS f32x4*)(w + 4 * EH), w1 = *(const GAS f32x4*)(w + 768 + 4 * EH), w2 = *(const GAS f32x4*)(w + 1536 + 4 * EH), bs = *(const GAS f32x4*)(bias + 4 * EH);
; #pragma unroll
;     for (int e = 0; e < 4; ++e)
; #pragma unroll
;         for (int i = 0; i < 4; ++i) u[i][e] = bfe(rows[i], 4 * EH + e) * w0[e] + bfe(rows[i + 1], 4 * EH + e) * w1[e] + bfe(rows[i + 2], 4 * EH + e) * w2[e] + bs[e];
; }
; template <int EH> __device__ __forceinline__ void hy_z_half(const v4u (&r1)[6], const v4u (&r2)[6], const GAS float* cw, const GAS float* cb, unsigned (&zp)[4][4]) {
;     float x1[4][4], vv[4][4]; hy_conv4x4<EH>(r1, cw + 256, cb + 256, x1); hy_conv4x4<EH>(r2, cw + 512, cb + 512, vv);
; #pragma unroll
;     for (int i = 0; i < 4; ++i) { zp[i][2 * EH] = pk2(x1[i][0] * vv[i][0], x1[i][1] * vv[i][1]); zp[i][2 * EH + 1] = pk2(x1[i][2] * vv[i][2], x1[i][3] * vv[i][3]); }
.LBB0_467:
	s_or_b64 exec, exec, s[0:1]
	s_add_u32 s2, s26, s10
	s_addc_u32 s3, s27, s11
	s_add_u32 s0, s24, s12
	v_lshlrev_b32_e32 v182, 2, v88
	s_addc_u32 s1, s25, s13
	v_lshl_add_u64 v[62:63], s[0:1], 0, v[182:183]
	v_add_co_u32_e32 v84, vcc, s71, v62
	global_load_dwordx4 v[54:57], v182, s[2:3] offset:1024
	global_load_dwordx4 v[50:53], v182, s[2:3] offset:2048
	global_load_dwordx4 v[58:61], v182, s[0:1] offset:1024
	v_addc_co_u32_e32 v85, vcc, 0, v63, vcc
	v_add_co_u32_e32 v82, vcc, s64, v62
	v_addc_co_u32_e32 v83, vcc, 0, v63, vcc
	global_load_dwordx4 v[70:73], v[82:83], off offset:-4096
	global_load_dwordx4 v[62:65], v[84:85], off offset:3072
	global_load_dwordx4 v[66:69], v182, s[0:1] offset:2048
	global_load_dwordx4 v[74:77], v[84:85], off offset:1024
	global_load_dwordx4 v[78:81], v[82:83], off
	s_waitcnt vmcnt(5)
	v_lshlrev_b32_e32 v92, 16, v38
	v_and_b32_e32 v93, 0xffff0000, v38
	v_lshlrev_b32_e32 v90, 16, v26
	v_and_b32_e32 v91, 0xffff0000, v26
	v_lshlrev_b32_e32 v96, 16, v34
	v_and_b32_e32 v97, 0xffff0000, v34
	v_lshlrev_b32_e32 v98, 16, v46
	v_and_b32_e32 v99, 0xffff0000, v46
	v_lshlrev_b32_e32 v102, 16, v30
	v_and_b32_e32 v103, 0xffff0000, v30
	v_lshlrev_b32_e32 v104, 16, v22
	v_and_b32_e32 v105, 0xffff0000, v22
	v_lshlrev_b32_e32 v108, 16, v18
	v_and_b32_e32 v109, 0xffff0000, v18
	v_lshlrev_b32_e32 v114, 16, v2
	v_and_b32_e32 v115, 0xffff0000, v2
	v_lshlrev_b32_e32 v116, 16, v14
	v_and_b32_e32 v117, 0xffff0000, v14
	v_lshlrev_b32_e32 v38, 16, v39
	v_and_b32_e32 v39, 0xffff0000, v39
	v_lshlrev_b32_e32 v26, 16, v27
	v_and_b32_e32 v27, 0xffff0000, v27
	v_lshlrev_b32_e32 v34, 16, v35
	v_and_b32_e32 v35, 0xffff0000, v35
	v_lshlrev_b32_e32 v46, 16, v47
	v_and_b32_e32 v47, 0xffff0000, v47
	v_lshlrev_b32_e32 v30, 16, v31
	v_and_b32_e32 v31, 0xffff0000, v31
	v_lshlrev_b32_e32 v2, 16, v3
	v_and_b32_e32 v3, 0xffff0000, v3
	s_waitcnt vmcnt(4)
	v_pk_mul_f32 v[94:95], v[70:71], v[92:93]
	s_nop 0
	v_pk_fma_f32 v[94:95], v[58:59], v[90:91], v[94:95]
	v_pk_mul_f32 v[106:107], v[70:71], v[90:91]
	s_waitcnt vmcnt(3)
	v_pk_fma_f32 v[94:95], v[62:63], v[96:97], v[94:95]
	v_lshlrev_b32_e32 v96, 16, v42
	v_and_b32_e32 v97, 0xffff0000, v42
	s_waitcnt vmcnt(1)
	v_pk_mul_f32 v[100:101], v[74:75], v[98:99]
	v_pk_mul_f32 v[112:113], v[74:75], v[104:105]
	v_pk_fma_f32 v[100:101], v[66:67], v[96:97], v[100:101]
	v_pk_fma_f32 v[112:113], v[66:67], v[108:109], v[112:113]
	s_waitcnt vmcnt(0)
	v_pk_fma_f32 v[100:101], v[78:79], v[102:103], v[100:101]
	v_lshlrev_b32_e32 v102, 16, v10
	v_and_b32_e32 v103, 0xffff0000, v10
	v_pk_fma_f32 v[106:107], v[58:59], v[102:103], v[106:107]
	v_pk_mul_f32 v[110:111], v[70:71], v[102:103]
	v_pk_fma_f32 v[92:93], v[62:63], v[92:93], v[106:107]
	v_pk_mul_f32 v[106:107], v[74:75], v[96:97]
	v_pk_add_f32 v[94:95], v[54:55], v[94:95]
	v_pk_fma_f32 v[106:107], v[66:67], v[104:105], v[106:107]
	v_pk_add_f32 v[92:93], v[54:55], v[92:93]
	v_pk_fma_f32 v[98:99], v[78:79], v[98:99], v[106:107]
	v_lshlrev_b32_e32 v106, 16, v6
	v_and_b32_e32 v107, 0xffff0000, v6
	v_pk_mul_f32 v[70:71], v[70:71], v[106:107]
	v_pk_fma_f32 v[110:111], v[58:59], v[106:107], v[110:111]
	v_pk_fma_f32 v[58:59], v[58:59], v[114:115], v[70:71]
	v_pk_mul_f32 v[70:71], v[74:75], v[108:109]
	v_pk_fma_f32 v[58:59], v[62:63], v[102:103], v[58:59]
	v_pk_fma_f32 v[66:67], v[66:67], v[116:117], v[70:71]
	v_pk_add_f32 v[58:59], v[54:55], v[58:59]
	v_pk_fma_f32 v[66:67], v[78:79], v[104:105], v[66:67]
	v_pk_add_f32 v[100:101], v[50:51], v[100:101]
	v_pk_add_f32 v[66:67], v[50:51], v[66:67]
	v_pk_add_f32 v[98:99], v[50:51], v[98:99]
	v_pk_mul_f32 v[58:59], v[58:59], v[66:67]
	v_lshlrev_b32_e32 v42, 16, v43
	v_cvt_pk_bf16_f32 v10, v58, v59
	v_pk_fma_f32 v[58:59], v[62:63], v[90:91], v[110:111]
	v_and_b32_e32 v43, 0xffff0000, v43
	v_pk_add_f32 v[54:55], v[54:55], v[58:59]
	v_pk_fma_f32 v[58:59], v[78:79], v[96:97], v[112:113]
	v_lshlrev_b32_e32 v6, 16, v7
	v_pk_add_f32 v[50:51], v[50:51], v[58:59]
	v_pk_mul_f32 v[58:59], v[72:73], v[26:27]
	v_pk_mul_f32 v[50:51], v[54:55], v[50:51]
	v_lshlrev_b32_e32 v54, 16, v23
	v_cvt_pk_bf16_f32 v14, v50, v51
	v_pk_mul_f32 v[50:51], v[92:93], v[98:99]
	v_and_b32_e32 v55, 0xffff0000, v23
	v_cvt_pk_bf16_f32 v18, v50, v51
	v_pk_mul_f32 v[50:51], v[94:95], v[100:101]
	v_and_b32_e32 v7, 0xffff0000, v7
	v_cvt_pk_bf16_f32 v22, v50, v51
	v_pk_mul_f32 v[50:51], v[72:73], v[38:39]
	v_lshlrev_b32_e32 v70, 16, v15
	v_pk_fma_f32 v[50:51], v[60:61], v[26:27], v[50:51]
	v_and_b32_e32 v71, 0xffff0000, v15
	v_pk_fma_f32 v[34:35], v[64:65], v[34:35], v[50:51]
	v_pk_mul_f32 v[50:51], v[76:77], v[46:47]
	v_pk_mul_f32 v[66:67], v[76:77], v[54:55]
	v_pk_fma_f32 v[50:51], v[68:69], v[42:43], v[50:51]
	v_pk_add_f32 v[34:35], v[56:57], v[34:35]
	v_pk_fma_f32 v[30:31], v[80:81], v[30:31], v[50:51]
	v_lshlrev_b32_e32 v50, 16, v11
	v_and_b32_e32 v51, 0xffff0000, v11
	v_pk_fma_f32 v[58:59], v[60:61], v[50:51], v[58:59]
	v_pk_mul_f32 v[62:63], v[72:73], v[50:51]
	v_pk_fma_f32 v[38:39], v[64:65], v[38:39], v[58:59]
	v_pk_mul_f32 v[58:59], v[76:77], v[42:43]
	v_pk_fma_f32 v[62:63], v[60:61], v[6:7], v[62:63]
	v_pk_fma_f32 v[58:59], v[68:69], v[54:55], v[58:59]
	v_pk_mul_f32 v[6:7], v[72:73], v[6:7]
	v_pk_fma_f32 v[46:47], v[80:81], v[46:47], v[58:59]
	v_lshlrev_b32_e32 v58, 16, v19
	v_and_b32_e32 v59, 0xffff0000, v19
	v_pk_fma_f32 v[2:3], v[60:61], v[2:3], v[6:7]
	v_pk_mul_f32 v[6:7], v[76:77], v[58:59]
	v_pk_fma_f32 v[2:3], v[64:65], v[50:51], v[2:3]
	v_pk_fma_f32 v[6:7], v[68:69], v[70:71], v[6:7]
	v_pk_add_f32 v[2:3], v[56:57], v[2:3]
	v_pk_fma_f32 v[6:7], v[80:81], v[54:55], v[6:7]
	v_pk_fma_f32 v[66:67], v[68:69], v[58:59], v[66:67]
	v_pk_add_f32 v[6:7], v[52:53], v[6:7]
; #define GAS __attribute__((address_space(1)))
; __device__ __forceinline__ unsigned pk2(float lo, float hi) { const m_f32x2 v = {lo, hi}; return __builtin_bit_cast(unsigned, __builtin_convertvector(v, m_bf16x2)); }
; __device__ __forceinline__ float bfe(const v4u& w, int e) { const unsigned u = (e & 1) ? (w[e >> 1] & 0xffff0000u) : (w[e >> 1] << 16); return __uint_as_float(u); }
; template <int EH> __device__ __forceinline__ void hy_conv4x4(const v4u (&rows)[6], const GAS float* w, const GAS float* bias, float (&u)[4][4]) {
;     const f32x4 w0 = *(const GAS f32x4*)(w + 4 * EH), w1 = *(const GAS f32x4*)(w + 768 + 4 * EH), w2 = *(const GAS f32x4*)(w + 1536 + 4 * EH), bs = *(const GAS f32x4*)(bias + 4 * EH);
; #pragma unroll
;     for (int e = 0; e < 4; ++e)
; #pragma unroll
;         for (int i = 0; i < 4; ++i) u[i][e] = bfe(rows[i], 4 * EH + e) * w0[e] + bfe(rows[i + 1], 4 * EH + e) * w1[e] + bfe(rows[i + 2], 4 * EH + e) * w2[e] + bs[e];
; }
; template <int EH> __device__ __forceinline__ void hy_z_half(const v4u (&r1)[6], const v4u (&r2)[6], const GAS float* cw, const GAS float* cb, unsigned (&zp)[4][4]) {
;     float x1[4][4], vv[4][4]; hy_conv4x4<EH>(r1, cw + 256, cb + 256, x1); hy_conv4x4<EH>(r2, cw + 512, cb + 512, vv);
; #pragma unroll
;     for (int i = 0; i < 4; ++i) { zp[i][2 * EH] = pk2(x1[i][0] * vv[i][0], x1[i][1] * vv[i][1]); zp[i][2 * EH + 1] = pk2(x1[i][2] * vv[i][2], x1[i][3] * vv[i][3]); }
	v_pk_add_f32 v[38:39], v[56:57], v[38:39]
	v_pk_mul_f32 v[2:3], v[2:3], v[6:7]
	v_pk_fma_f32 v[6:7], v[80:81], v[42:43], v[66:67]
	v_cvt_pk_bf16_f32 v11, v2, v3
	v_pk_fma_f32 v[2:3], v[64:65], v[26:27], v[62:63]
	v_pk_add_f32 v[6:7], v[52:53], v[6:7]
	v_pk_add_f32 v[2:3], v[56:57], v[2:3]
	v_pk_add_f32 v[46:47], v[52:53], v[46:47]
	v_pk_mul_f32 v[2:3], v[2:3], v[6:7]
	v_pk_add_f32 v[30:31], v[52:53], v[30:31]
	v_cvt_pk_bf16_f32 v15, v2, v3
	v_pk_mul_f32 v[2:3], v[38:39], v[46:47]
	s_nop 0
	v_cvt_pk_bf16_f32 v19, v2, v3
	v_pk_mul_f32 v[2:3], v[34:35], v[30:31]
	s_nop 0
	v_cvt_pk_bf16_f32 v23, v2, v3
	global_load_dwordx4 v[54:57], v182, s[2:3] offset:1040
	global_load_dwordx4 v[50:53], v182, s[2:3] offset:2064
	global_load_dwordx4 v[58:61], v182, s[0:1] offset:1040
	global_load_dwordx4 v[70:73], v[84:85], off offset:16
	global_load_dwordx4 v[62:65], v[84:85], off offset:3088
	global_load_dwordx4 v[66:69], v182, s[0:1] offset:2064
	global_load_dwordx4 v[74:77], v[84:85], off offset:1040
	global_load_dwordx4 v[78:81], v[82:83], off offset:16
	v_lshlrev_b32_e32 v6, 16, v40
	v_and_b32_e32 v7, 0xffff0000, v40
	v_lshlrev_b32_e32 v2, 16, v28
	v_and_b32_e32 v3, 0xffff0000, v28
	v_lshlrev_b32_e32 v30, 16, v36
	v_and_b32_e32 v31, 0xffff0000, v36
	v_lshlrev_b32_e32 v34, 16, v48
	v_and_b32_e32 v35, 0xffff0000, v48
	v_lshlrev_b32_e32 v42, 16, v32
	v_and_b32_e32 v43, 0xffff0000, v32
	v_lshlrev_b32_e32 v46, 16, v24
	v_and_b32_e32 v47, 0xffff0000, v24
	v_lshlrev_b32_e32 v84, 16, v20
	v_and_b32_e32 v85, 0xffff0000, v20
	v_lshlrev_b32_e32 v94, 16, v4
	v_and_b32_e32 v95, 0xffff0000, v4
	v_lshlrev_b32_e32 v96, 16, v16
	v_and_b32_e32 v97, 0xffff0000, v16
	v_lshlrev_b32_e32 v28, 16, v37
	v_lshlrev_b32_e32 v32, 16, v33
	v_and_b32_e32 v33, 0xffff0000, v33
	v_lshlrev_b32_e32 v24, 16, v25
	v_and_b32_e32 v25, 0xffff0000, v25
	v_lshlrev_b32_e32 v20, 16, v21
	v_and_b32_e32 v21, 0xffff0000, v21
	v_lshlrev_b32_e32 v4, 16, v5
	v_and_b32_e32 v5, 0xffff0000, v5
	v_lshlrev_b32_e32 v16, 16, v17
	v_and_b32_e32 v17, 0xffff0000, v17
	s_waitcnt vmcnt(4)
	v_pk_mul_f32 v[26:27], v[70:71], v[6:7]
	s_nop 0
	v_pk_fma_f32 v[26:27], v[58:59], v[2:3], v[26:27]
	v_pk_mul_f32 v[82:83], v[70:71], v[2:3]
	s_waitcnt vmcnt(3)
	v_pk_fma_f32 v[26:27], v[62:63], v[30:31], v[26:27]
	v_lshlrev_b32_e32 v30, 16, v44
	v_and_b32_e32 v31, 0xffff0000, v44
	s_waitcnt vmcnt(1)
	v_pk_mul_f32 v[38:39], v[74:75], v[34:35]
	v_pk_mul_f32 v[92:93], v[74:75], v[46:47]
	v_pk_fma_f32 v[38:39], v[66:67], v[30:31], v[38:39]
	v_pk_fma_f32 v[92:93], v[66:67], v[84:85], v[92:93]
	s_waitcnt vmcnt(0)
; #define GAS __attribute__((address_space(1)))
; #define LAS __attribute__((address_space(3)))
; __device__ __forceinline__ unsigned pk2(float lo, float hi) { const m_f32x2 v = {lo, hi}; return __builtin_bit_cast(unsigned, __builtin_convertvector(v, m_bf16x2)); }
; template <int EH> __device__ __forceinline__ void hy_z_half(const v4u (&r1)[6], const v4u (&r2)[6], const GAS float* cw, const GAS float* cb, unsigned (&zp)[4][4]) {
;     float x1[4][4], vv[4][4]; hy_conv4x4<EH>(r1, cw + 256, cb + 256, x1); hy_conv4x4<EH>(r2, cw + 512, cb + 512, vv);
; #pragma unroll
;     for (int i = 0; i < 4; ++i) { zp[i][2 * EH] = pk2(x1[i][0] * vv[i][0], x1[i][1] * vv[i][1]); zp[i][2 * EH + 1] = pk2(x1[i][2] * vv[i][2], x1[i][3] * vv[i][3]); }
;     __builtin_amdgcn_sched_barrier(0);
; }
; __device__ __forceinline__ void hy_prep_item(Frame& F, int l, int item, LAS unsigned char* lb) {
;     int tid = F.tid; asm volatile("" : "+v"(tid));
;     const int b = item >> 6, t0 = (item & 63) * 64, cg = tid & 31, tq = tid >> 5, tq0 = t0 + 4 * tq;
;     const GAS bf16* p = (const GAS bf16*)(F.ws + WS_PROJ) + ((size_t)b * SEQ + tq0) * NPROJ + PC_HX1 + 8 * cg;
;     const GAS float* cw = INP(F, I_HCW) + l * 3 * 768 + 8 * cg; const GAS float* cb = INP(F, I_HCB) + l * 768 + 8 * cg;
;     v4u r1[6], r2[6]; hy_rows(p, tq0, r1); hy_rows(p + 256, tq0, r2);
;     unsigned zp[4][4]; hy_z_half<0>(r1, r2, cw, cb, zp); hy_z_half<1>(r1, r2, cw, cb, zp);
;     LAS bf16* zs = (LAS bf16*)lb;
; #pragma unroll
;     for (int e = 0; e < 8; ++e) { const int sh = (e & 1) * 16; v2u o;
;         o.x = ((zp[0][e >> 1] >> sh) & 0xffffu) | (((zp[1][e >> 1] >> sh) & 0xffffu) << 16); o.y = ((zp[2][e >> 1] >> sh) & 0xffffu) | (((zp[3][e >> 1] >> sh) & 0xffffu) << 16);
;         *(LAS v2u*)(zs + (8 * cg + e) * 72 + 4 * tq) = o; }
;     __syncthreads();
;     {   const int cc = tid >> 1, hh = tid & 1; GAS bf16* zt = (GAS bf16*)(F.ws + WS_ZT) + ((size_t)cc * BATCH + b) * SEQ + t0 + hh * 32;
; #pragma unroll
;         for (int q = 0; q < 4; ++q) *(GAS v4u*)(zt + 8 * q) = *(LAS v4u*)(zs + cc * 72 + hh * 32 + 8 * q); }
;     __syncthreads();
	v_pk_fma_f32 v[38:39], v[78:79], v[42:43], v[38:39]
	v_lshlrev_b32_e32 v42, 16, v12
	v_and_b32_e32 v43, 0xffff0000, v12
	v_pk_fma_f32 v[82:83], v[58:59], v[42:43], v[82:83]
	v_pk_mul_f32 v[90:91], v[70:71], v[42:43]
	v_pk_fma_f32 v[6:7], v[62:63], v[6:7], v[82:83]
	v_pk_mul_f32 v[82:83], v[74:75], v[30:31]
	v_pk_fma_f32 v[30:31], v[78:79], v[30:31], v[92:93]
	v_pk_fma_f32 v[82:83], v[66:67], v[46:47], v[82:83]
	v_pk_add_f32 v[30:31], v[50:51], v[30:31]
	v_pk_fma_f32 v[34:35], v[78:79], v[34:35], v[82:83]
	v_lshlrev_b32_e32 v82, 16, v8
	v_and_b32_e32 v83, 0xffff0000, v8
	v_pk_mul_f32 v[70:71], v[70:71], v[82:83]
	v_pk_fma_f32 v[90:91], v[58:59], v[82:83], v[90:91]
	v_pk_fma_f32 v[58:59], v[58:59], v[94:95], v[70:71]
	v_pk_mul_f32 v[70:71], v[74:75], v[84:85]
	v_pk_fma_f32 v[42:43], v[62:63], v[42:43], v[58:59]
	v_pk_fma_f32 v[66:67], v[66:67], v[96:97], v[70:71]
	v_pk_fma_f32 v[2:3], v[62:63], v[2:3], v[90:91]
	v_pk_fma_f32 v[46:47], v[78:79], v[46:47], v[66:67]
	v_pk_add_f32 v[42:43], v[54:55], v[42:43]
	v_pk_add_f32 v[46:47], v[50:51], v[46:47]
	v_pk_add_f32 v[2:3], v[54:55], v[2:3]
	v_pk_add_f32 v[6:7], v[54:55], v[6:7]
	v_pk_add_f32 v[34:35], v[50:51], v[34:35]
	v_pk_mul_f32 v[42:43], v[42:43], v[46:47]
	v_pk_mul_f32 v[2:3], v[2:3], v[30:31]
	v_pk_add_f32 v[26:27], v[54:55], v[26:27]
	v_pk_add_f32 v[38:39], v[50:51], v[38:39]
	v_cvt_pk_bf16_f32 v40, v42, v43
	v_cvt_pk_bf16_f32 v42, v2, v3
	v_pk_mul_f32 v[2:3], v[6:7], v[34:35]
	v_lshlrev_b32_e32 v30, 16, v49
	v_cvt_pk_bf16_f32 v43, v2, v3
	v_pk_mul_f32 v[2:3], v[26:27], v[38:39]
	v_lshlrev_b32_e32 v26, 16, v41
	v_and_b32_e32 v27, 0xffff0000, v41
	v_cvt_pk_bf16_f32 v38, v2, v3
	v_lshlrev_b32_e32 v2, 16, v29
	v_and_b32_e32 v3, 0xffff0000, v29
	v_pk_mul_f32 v[6:7], v[72:73], v[26:27]
	v_and_b32_e32 v29, 0xffff0000, v37
	v_pk_fma_f32 v[6:7], v[60:61], v[2:3], v[6:7]
	v_and_b32_e32 v31, 0xffff0000, v49
	v_pk_fma_f32 v[6:7], v[64:65], v[28:29], v[6:7]
	v_lshlrev_b32_e32 v28, 16, v45
	v_and_b32_e32 v29, 0xffff0000, v45
	v_pk_mul_f32 v[34:35], v[76:77], v[30:31]
	v_lshlrev_b32_e32 v12, 16, v13
	v_pk_fma_f32 v[34:35], v[68:69], v[28:29], v[34:35]
	v_and_b32_e32 v13, 0xffff0000, v13
	v_pk_fma_f32 v[32:33], v[80:81], v[32:33], v[34:35]
	v_pk_mul_f32 v[34:35], v[72:73], v[2:3]
	v_lshlrev_b32_e32 v8, 16, v9
	v_pk_fma_f32 v[34:35], v[60:61], v[12:13], v[34:35]
	v_and_b32_e32 v9, 0xffff0000, v9
	v_pk_fma_f32 v[26:27], v[64:65], v[26:27], v[34:35]
	v_pk_mul_f32 v[34:35], v[76:77], v[28:29]
	v_pk_mul_f32 v[36:37], v[76:77], v[24:25]
	v_pk_fma_f32 v[34:35], v[68:69], v[24:25], v[34:35]
	v_pk_fma_f32 v[36:37], v[68:69], v[20:21], v[36:37]
	v_pk_fma_f32 v[30:31], v[80:81], v[30:31], v[34:35]
	v_pk_mul_f32 v[34:35], v[72:73], v[12:13]
	v_pk_add_f32 v[26:27], v[56:57], v[26:27]
	v_pk_fma_f32 v[34:35], v[60:61], v[8:9], v[34:35]
	v_pk_mul_f32 v[8:9], v[72:73], v[8:9]
	v_pk_fma_f32 v[2:3], v[64:65], v[2:3], v[34:35]
	v_pk_fma_f32 v[4:5], v[60:61], v[4:5], v[8:9]
	v_pk_mul_f32 v[8:9], v[76:77], v[20:21]
	v_pk_fma_f32 v[4:5], v[64:65], v[12:13], v[4:5]
	v_pk_fma_f32 v[8:9], v[68:69], v[16:17], v[8:9]
	v_pk_add_f32 v[4:5], v[56:57], v[4:5]
	v_pk_fma_f32 v[8:9], v[80:81], v[24:25], v[8:9]
	v_pk_add_f32 v[2:3], v[56:57], v[2:3]
	v_pk_add_f32 v[8:9], v[52:53], v[8:9]
	v_pk_add_f32 v[30:31], v[52:53], v[30:31]
	v_pk_mul_f32 v[4:5], v[4:5], v[8:9]
	v_pk_add_f32 v[6:7], v[56:57], v[6:7]
	v_cvt_pk_bf16_f32 v8, v4, v5
	v_pk_fma_f32 v[4:5], v[80:81], v[28:29], v[36:37]
	v_pk_add_f32 v[32:33], v[52:53], v[32:33]
	v_pk_add_f32 v[4:5], v[52:53], v[4:5]
	s_nop 0
	v_pk_mul_f32 v[2:3], v[2:3], v[4:5]
	s_nop 0
	v_cvt_pk_bf16_f32 v9, v2, v3
	v_pk_mul_f32 v[2:3], v[26:27], v[30:31]
	s_nop 0
	v_cvt_pk_bf16_f32 v12, v2, v3
	v_pk_mul_f32 v[2:3], v[6:7], v[32:33]
	s_nop 0
	v_cvt_pk_bf16_f32 v6, v2, v3
	v_lshlrev_b32_e32 v4, 1, v87
	v_mul_u32_u24_e32 v5, 0x90, v88
	v_and_b32_e32 v2, 0xffff, v10
	v_lshlrev_b32_e32 v3, 16, v22
	s_mov_b32 s0, 0xffff
	v_add3_u32 v7, 0, v4, v5
	v_lshrrev_b32_e32 v4, 16, v10
	v_lshrrev_b32_e32 v5, 16, v18
	v_lshl_or_b32 v2, v14, 16, v2
	v_and_or_b32 v3, v18, s0, v3
	v_and_or_b32 v4, v14, s38, v4
	v_and_or_b32 v5, v22, s38, v5
	v_add_u32_e32 v7, 0x2000, v7
	ds_write2_b64 v7, v[2:3], v[4:5] offset0:64 offset1:82
	v_and_b32_e32 v2, 0xffff, v11
	v_lshlrev_b32_e32 v3, 16, v23
	v_lshrrev_b32_e32 v4, 16, v11
	v_lshrrev_b32_e32 v5, 16, v19
	v_lshl_or_b32 v2, v15, 16, v2
	v_and_or_b32 v3, v19, s0, v3
	v_and_or_b32 v4, v15, s38, v4
	v_and_or_b32 v5, v23, s38, v5
	ds_write2_b64 v7, v[2:3], v[4:5] offset0:100 offset1:118
	v_and_b32_e32 v2, 0xffff, v40
	v_lshlrev_b32_e32 v3, 16, v38
	v_lshrrev_b32_e32 v4, 16, v40
	v_lshrrev_b32_e32 v5, 16, v43
	v_lshl_or_b32 v2, v42, 16, v2
	v_and_or_b32 v3, v43, s0, v3
	v_and_or_b32 v4, v42, s38, v4
	v_and_or_b32 v5, v38, s38, v5
	ds_write2_b64 v7, v[2:3], v[4:5] offset0:136 offset1:154
	v_and_b32_e32 v2, 0xffff, v8
	v_lshlrev_b32_e32 v3, 16, v6
	v_lshrrev_b32_e32 v4, 16, v8
	v_lshrrev_b32_e32 v5, 16, v12
	v_lshl_or_b32 v2, v9, 16, v2
	v_and_or_b32 v3, v12, s0, v3
	v_and_or_b32 v4, v9, s38, v4
	v_and_or_b32 v5, v6, s38, v5
	ds_write2_b64 v7, v[2:3], v[4:5] offset0:172 offset1:190
	v_ashrrev_i32_e32 v2, 1, v86
	v_ashrrev_i32_e32 v3, 31, v2
	v_lshlrev_b64 v[4:5], 15, v[2:3]
	v_lshl_add_u64 v[4:5], s[8:9], 0, v[4:5]
	s_lshl_b64 s[0:1], s[14:15], 13
	v_lshlrev_b32_e32 v3, 6, v86
	v_lshl_add_u64 v[4:5], v[4:5], 0, s[0:1]
	s_lshl_b32 s94, s23, 1
	v_and_b32_e32 v182, 64, v3
	v_mul_lo_u32 v2, v2, s65
	v_lshl_add_u64 v[4:5], v[4:5], 0, s[94:95]
	v_add3_u32 v14, 0, v2, v182
	s_waitcnt lgkmcnt(0)
	s_barrier
	v_lshl_add_u64 v[18:19], v[4:5], 0, v[182:183]
	ds_read_b128 v[2:5], v14 offset:8704
	ds_read_b128 v[6:9], v14 offset:8720
	ds_read_b128 v[10:13], v14 offset:8736
	ds_read_b128 v[14:17], v14 offset:8752
	s_add_i32 s22, s22, s34
	s_add_i32 s19, s19, s18
	s_cmpk_gt_i32 s22, 0xff
	s_waitcnt lgkmcnt(3)
	global_store_dwordx4 v[18:19], v[2:5], off
	s_waitcnt lgkmcnt(2)
	global_store_dwordx4 v[18:19], v[6:9], off offset:16
	s_waitcnt lgkmcnt(1)
	global_store_dwordx4 v[18:19], v[10:13], off offset:32
	s_waitcnt lgkmcnt(0)
	global_store_dwordx4 v[18:19], v[14:17], off offset:48
	s_barrier
	s_cbranch_scc1 .LBB0_492
